# grid barrier: the workgroup arriving third from last on its XCD issues an early L2 write-back so the leader's release write-back has little left
# speedup vs baseline: 1.0003x; 1.0003x over previous
.LBB0_171:
	s_or_b64 exec, exec, s[8:9]
	v_cvt_f32_u32_e32 v4, v2
	s_waitcnt vmcnt(0)
	v_readfirstlane_b32 s4, v3
	v_sub_u32_e32 v3, 0, v2
	v_rcp_iflag_f32_e32 v4, v4
	v_add_u32_e32 v5, s4, v1
	v_mul_f32_e32 v4, 0x4f7ffffe, v4
	v_cvt_u32_f32_e32 v4, v4
	v_mul_lo_u32 v1, v3, v4
	v_mul_hi_u32 v1, v4, v1
	v_add_u32_e32 v1, v4, v1
	v_mul_hi_u32 v1, v5, v1
	v_mul_lo_u32 v3, v1, v2
	v_sub_u32_e32 v3, v5, v3
	v_add_u32_e32 v4, 1, v1
	v_cmp_ge_u32_e32 vcc, v3, v2
	s_nop 1
	v_cndmask_b32_e32 v1, v1, v4, vcc
	v_sub_u32_e32 v4, v3, v2
	v_cndmask_b32_e32 v3, v3, v4, vcc
	v_add_u32_e32 v4, 1, v1
	v_cmp_ge_u32_e32 vcc, v3, v2
	v_add_u32_e32 v3, 1, v5
	s_nop 0
	v_cndmask_b32_e32 v1, v1, v4, vcc
	v_mul_lo_u32 v4, v2, v1
	v_add_u32_e32 v2, v4, v2
	v_cmp_ne_u32_e32 vcc, v3, v2
	s_and_saveexec_b64 s[4:5], vcc
	s_xor_b64 s[6:7], exec, s[4:5]
	s_cbranch_execz .LBB0_185
	v_add_u32_e32 v100, 2, v3
	v_cmp_eq_u32_e32 vcc, v100, v2
	s_cbranch_vccz .Lpf_0
	buffer_wbl2 sc1

.LBB0_289:
	s_or_b64 exec, exec, s[6:7]
	v_cvt_f32_u32_e32 v5, v3
	s_waitcnt vmcnt(0)
	v_readfirstlane_b32 s4, v4
	v_sub_u32_e32 v4, 0, v3
	v_rcp_iflag_f32_e32 v5, v5
	v_add_u32_e32 v6, s4, v0
	v_mul_f32_e32 v5, 0x4f7ffffe, v5
	v_cvt_u32_f32_e32 v5, v5
	v_mul_lo_u32 v0, v4, v5
	v_mul_hi_u32 v0, v5, v0
	v_add_u32_e32 v0, v5, v0
	v_mul_hi_u32 v0, v6, v0
	v_mul_lo_u32 v4, v0, v3
	v_sub_u32_e32 v4, v6, v4
	v_add_u32_e32 v5, 1, v0
	v_cmp_ge_u32_e32 vcc, v4, v3
	s_nop 1
	v_cndmask_b32_e32 v0, v0, v5, vcc
	v_sub_u32_e32 v5, v4, v3
	v_cndmask_b32_e32 v4, v4, v5, vcc
	v_add_u32_e32 v5, 1, v0
	v_cmp_ge_u32_e32 vcc, v4, v3
	v_add_u32_e32 v4, 1, v6
	s_nop 0
	v_cndmask_b32_e32 v0, v0, v5, vcc
	v_mul_lo_u32 v5, v3, v0
	v_add_u32_e32 v3, v5, v3
	v_cmp_ne_u32_e32 vcc, v4, v3
	s_and_saveexec_b64 s[4:5], vcc
	s_xor_b64 s[4:5], exec, s[4:5]
	s_cbranch_execz .LBB0_303
	v_add_u32_e32 v100, 2, v4
	v_cmp_eq_u32_e32 vcc, v100, v3
	s_cbranch_vccz .Lpf_4
	buffer_wbl2 sc1

.LBB0_628:
	s_or_b64 exec, exec, s[6:7]
	v_cvt_f32_u32_e32 v5, v3
	s_waitcnt vmcnt(0)
	v_readfirstlane_b32 s2, v4
	v_sub_u32_e32 v4, 0, v3
	v_rcp_iflag_f32_e32 v5, v5
	v_add_u32_e32 v6, s2, v0
	v_mul_f32_e32 v5, 0x4f7ffffe, v5
	v_cvt_u32_f32_e32 v5, v5
	v_mul_lo_u32 v0, v4, v5
	v_mul_hi_u32 v0, v5, v0
	v_add_u32_e32 v0, v5, v0
	v_mul_hi_u32 v0, v6, v0
	v_mul_lo_u32 v4, v0, v3
	v_sub_u32_e32 v4, v6, v4
	v_add_u32_e32 v5, 1, v0
	v_cmp_ge_u32_e32 vcc, v4, v3
	s_nop 1
	v_cndmask_b32_e32 v0, v0, v5, vcc
	v_sub_u32_e32 v5, v4, v3
	v_cndmask_b32_e32 v4, v4, v5, vcc
	v_add_u32_e32 v5, 1, v0
	v_cmp_ge_u32_e32 vcc, v4, v3
	v_add_u32_e32 v4, 1, v6
	s_nop 0
	v_cndmask_b32_e32 v0, v0, v5, vcc
	v_mul_lo_u32 v5, v3, v0
	v_add_u32_e32 v3, v5, v3
	v_cmp_ne_u32_e32 vcc, v4, v3
	s_and_saveexec_b64 s[2:3], vcc
	s_xor_b64 s[2:3], exec, s[2:3]
	s_cbranch_execz .LBB0_642
	v_add_u32_e32 v100, 2, v4
	v_cmp_eq_u32_e32 vcc, v100, v3
	s_cbranch_vccz .Lpf_8
	buffer_wbl2 sc1

.LBB0_794:
	s_or_b64 exec, exec, s[10:11]
	v_cvt_f32_u32_e32 v5, v3
	s_waitcnt vmcnt(0)
	v_readfirstlane_b32 s6, v4
	v_sub_u32_e32 v4, 0, v3
	v_rcp_iflag_f32_e32 v5, v5
	v_add_u32_e32 v6, s6, v0
	v_mul_f32_e32 v5, 0x4f7ffffe, v5
	v_cvt_u32_f32_e32 v5, v5
	v_mul_lo_u32 v0, v4, v5
	v_mul_hi_u32 v0, v5, v0
	v_add_u32_e32 v0, v5, v0
	v_mul_hi_u32 v0, v6, v0
	v_mul_lo_u32 v4, v0, v3
	v_sub_u32_e32 v4, v6, v4
	v_add_u32_e32 v5, 1, v0
	v_cmp_ge_u32_e32 vcc, v4, v3
	s_nop 1
	v_cndmask_b32_e32 v0, v0, v5, vcc
	v_sub_u32_e32 v5, v4, v3
	v_cndmask_b32_e32 v4, v4, v5, vcc
	v_add_u32_e32 v5, 1, v0
	v_cmp_ge_u32_e32 vcc, v4, v3
	v_add_u32_e32 v4, 1, v6
	s_nop 0
	v_cndmask_b32_e32 v0, v0, v5, vcc
	v_mul_lo_u32 v5, v3, v0
	v_add_u32_e32 v3, v5, v3
	v_cmp_ne_u32_e32 vcc, v4, v3
	s_and_saveexec_b64 s[6:7], vcc
	s_xor_b64 s[6:7], exec, s[6:7]
	s_cbranch_execz .LBB0_808
	v_add_u32_e32 v100, 2, v4
	v_cmp_eq_u32_e32 vcc, v100, v3
	s_cbranch_vccz .Lpf_12
	buffer_wbl2 sc1

.LBB0_897:
	s_or_b64 exec, exec, s[4:5]
	v_cvt_f32_u32_e32 v5, v3
	s_waitcnt vmcnt(0)
	v_readfirstlane_b32 s2, v4
	v_sub_u32_e32 v4, 0, v3
	v_rcp_iflag_f32_e32 v5, v5
	v_add_u32_e32 v6, s2, v0
	v_mul_f32_e32 v5, 0x4f7ffffe, v5
	v_cvt_u32_f32_e32 v5, v5
	v_mul_lo_u32 v0, v4, v5
	v_mul_hi_u32 v0, v5, v0
	v_add_u32_e32 v0, v5, v0
	v_mul_hi_u32 v0, v6, v0
	v_mul_lo_u32 v4, v0, v3
	v_sub_u32_e32 v4, v6, v4
	v_add_u32_e32 v5, 1, v0
	v_cmp_ge_u32_e32 vcc, v4, v3
	s_nop 1
	v_cndmask_b32_e32 v0, v0, v5, vcc
	v_sub_u32_e32 v5, v4, v3
	v_cndmask_b32_e32 v4, v4, v5, vcc
	v_add_u32_e32 v5, 1, v0
	v_cmp_ge_u32_e32 vcc, v4, v3
	v_add_u32_e32 v4, 1, v6
	s_nop 0
	v_cndmask_b32_e32 v0, v0, v5, vcc
	v_mul_lo_u32 v5, v3, v0
	v_add_u32_e32 v3, v5, v3
	v_cmp_ne_u32_e32 vcc, v4, v3
	s_and_saveexec_b64 s[2:3], vcc
	s_xor_b64 s[2:3], exec, s[2:3]
	s_cbranch_execz .LBB0_911
	v_add_u32_e32 v100, 2, v4
	v_cmp_eq_u32_e32 vcc, v100, v3
	s_cbranch_vccz .Lpf_16
	buffer_wbl2 sc1
